# baseline (speedup 1.0000x reference)
_ZN12_GLOBAL__N_111attn_kernelEPKDF16_S1_S1_PKiPDF16_:
	s_load_dwordx8 s[4:11], s[0:1], 0x0
	s_lshr_b32 s68, s2, 6
	s_and_b32 s33, s2, 7
	s_bfe_u32 s83, s2, 0x30003
	s_lshl_b32 s2, s68, 2
	s_waitcnt lgkmcnt(0)
	s_load_dword s64, s[10:11], s2 offset:0x0
	s_mov_b32 s69, 0
	s_lshl_b32 s2, s68, 3
	s_or_b32 s2, s2, s33
	v_readfirstlane_b32 s66, v0
	s_mov_b32 s3, s69
	s_lshl_b64 s[10:11], s[2:3], 6
	s_lshl_b32 s3, s83, 3
	s_lshr_b32 s82, s66, 6
	s_cmp_lt_u32 s82, 4
	s_cbranch_scc0 .Lmy_prio_done
	s_setprio 1
.Lmy_prio_done:
	s_or_b32 s3, s10, s3
	s_add_u32 s10, s3, s82
	s_addc_u32 s11, s11, 0
	s_lshl_b64 s[10:11], s[10:11], 12
	s_add_u32 s4, s4, s10
	s_addc_u32 s5, s5, s11
	s_mul_hi_u32 s3, s2, 0x48000
	s_mul_i32 s2, s2, 0x48000
	s_add_u32 s6, s6, s2
	s_addc_u32 s7, s7, s3
	s_lshl_b32 s65, s82, 10
	s_add_u32 s74, s6, s65
	s_addc_u32 s75, s7, 0
	s_add_u32 s2, s8, s2
	s_addc_u32 s3, s9, s3
	s_add_u32 s72, s2, s65
	s_addc_u32 s73, s3, 0
	s_cmp_lg_u32 0, -1
	v_and_b32_e32 v198, 63, v0
	s_cselect_b32 s2, 0, 0
	v_bfe_u32 v200, v0, 5, 1
	v_lshlrev_b32_e32 v205, 4, v198
	s_add_i32 s88, s65, s2
	s_mov_b32 s2, m0
	s_mov_b32 m0, s88
	s_nop 0
	global_load_lds_dwordx4 v205, s[74:75]
	s_mov_b32 m0, s2
	v_and_b32_e32 v199, 31, v0
	s_add_i32 s87, s88, 0x6000
	s_mov_b32 s2, m0
	s_mov_b32 m0, s87
	s_nop 0
	global_load_lds_dwordx4 v205, s[72:73]
	s_mov_b32 m0, s2
	v_lshlrev_b32_e32 v196, 9, v200
	v_mov_b32_e32 v197, 0
	v_lshlrev_b32_e32 v18, 4, v199
	s_add_u32 s2, s74, 0x2000
	v_lshl_add_u64 v[2:3], s[4:5], 0, v[196:197]
	v_mov_b32_e32 v19, v197
	s_addc_u32 s3, s75, 0
	s_add_i32 s6, s88, 0x2000
	s_mov_b32 s7, m0
	s_mov_b32 m0, s6
	s_nop 0
	global_load_lds_dwordx4 v205, s[2:3]
	s_mov_b32 m0, s7
	v_lshl_add_u64 v[12:13], v[2:3], 0, v[18:19]
	global_load_dwordx4 v[140:143], v[12:13], off
	global_load_dwordx4 v[136:139], v[12:13], off offset:1024
	global_load_dwordx4 v[132:135], v[12:13], off offset:2048
	global_load_dwordx4 v[128:131], v[12:13], off offset:3072
	v_mov_b32_e32 v2, v197
	v_mov_b32_e32 v3, v197
	v_mov_b32_e32 v4, v197
	v_mov_b32_e32 v5, v197
	v_mov_b32_e32 v6, v197
	v_mov_b32_e32 v7, v197
	v_mov_b32_e32 v8, v197
	v_mov_b32_e32 v9, v197
	v_mov_b32_e32 v10, v197
	v_mov_b32_e32 v11, v197
	v_mov_b32_e32 v12, v197
	v_mov_b32_e32 v13, v197
	v_mov_b32_e32 v14, v197
	v_mov_b32_e32 v15, v197
	v_mov_b32_e32 v16, v197
	v_mov_b32_e32 v17, v197
	s_add_u32 s2, s74, 0x4000
	v_lshlrev_b32_e32 v1, 10, v200
	s_addc_u32 s3, s75, 0
	s_add_i32 s4, s88, 0x4000
	s_mov_b32 s5, m0
	s_mov_b32 m0, s4
	s_nop 0
	global_load_lds_dwordx4 v205, s[2:3]
	s_mov_b32 m0, s5
	v_add3_u32 v207, 0, v1, v18
	s_waitcnt vmcnt(3) lgkmcnt(0)
	s_barrier
	s_add_i32 s100, s64, 63
	s_ashr_i32 s101, s100, 31
	s_lshr_b32 s101, s101, 26
	s_add_i32 s100, s100, s101
	s_ashr_i32 s89, s100, 6
	s_add_i32 s86, s89, -1
	s_lshl_b32 s100, s86, 6
	s_sub_i32 s85, s64, s100
	ds_read_b128 v[34:37], v207
	ds_read_b128 v[38:41], v207 offset:512
	s_add_i32 s2, s64, -1
	v_lshlrev_b32_e32 v1, 8, v200
	s_movk_i32 s90, 0x2000
	s_mov_b64 s[76:77], 0x4000
	s_movk_i32 s80, 0x4000
	s_cmp_gt_u32 s2, 63
	s_waitcnt vmcnt(3) lgkmcnt(1)
	v_mfma_f32_32x32x16_f16 v[18:33], v[34:37], v[140:143], v[2:17]
	s_waitcnt lgkmcnt(0)
	v_mfma_f32_32x32x16_f16 v[2:17], v[38:41], v[140:143], v[2:17]
	ds_read_b128 v[34:37], v207 offset:2048
	ds_read_b128 v[38:41], v207 offset:2560
	s_waitcnt vmcnt(2) lgkmcnt(1)
	v_mfma_f32_32x32x16_f16 v[18:33], v[34:37], v[136:139], v[18:33]
	s_waitcnt lgkmcnt(0)
	v_mfma_f32_32x32x16_f16 v[2:17], v[38:41], v[136:139], v[2:17]
	ds_read_b128 v[34:37], v207 offset:4096
	ds_read_b128 v[38:41], v207 offset:4608
	s_waitcnt vmcnt(1) lgkmcnt(1)
	v_mfma_f32_32x32x16_f16 v[18:33], v[34:37], v[132:135], v[18:33]
	s_waitcnt lgkmcnt(0)
	v_mfma_f32_32x32x16_f16 v[2:17], v[38:41], v[132:135], v[2:17]
	ds_read_b128 v[34:37], v207 offset:6144
	ds_read_b128 v[38:41], v207 offset:6656
	s_waitcnt vmcnt(0) lgkmcnt(1)
	v_mfma_f32_32x32x16_f16 v[18:33], v[34:37], v[128:131], v[18:33]
	s_waitcnt lgkmcnt(0)
	v_mfma_f32_32x32x16_f16 v[2:17], v[38:41], v[128:131], v[2:17]
	s_nop 15
	s_nop 7
	s_cbranch_scc1 .LBB3_2
	v_lshlrev_b32_e32 v34, 2, v200
	v_or_b32_e32 v35, 32, v34
	v_cmp_gt_i32_e32 vcc, s85, v35
	v_or_b32_e32 v35, 1, v34
	v_cmp_gt_i32_e64 s[30:31], s85, v35
	v_or_b32_e32 v35, 33, v34
	v_cmp_gt_i32_e64 s[2:3], s85, v35
	v_or_b32_e32 v35, 2, v34
	v_cmp_gt_i32_e64 s[36:37], s85, v35
	v_or_b32_e32 v35, 34, v34
	v_cmp_gt_i32_e64 s[4:5], s85, v35
	v_or_b32_e32 v35, 3, v34
	v_cmp_gt_i32_e64 s[38:39], s85, v35
	v_or_b32_e32 v35, 35, v34
	v_cmp_gt_i32_e64 s[6:7], s85, v35
	v_or_b32_e32 v35, 8, v34
	v_cmp_gt_i32_e64 s[40:41], s85, v35
	v_or_b32_e32 v35, 40, v34
	v_cmp_gt_i32_e64 s[8:9], s85, v35
	v_or_b32_e32 v35, 9, v34
	v_cmp_gt_i32_e64 s[42:43], s85, v35
	v_or_b32_e32 v35, 41, v34
	v_cmp_gt_i32_e64 s[10:11], s85, v35
	v_or_b32_e32 v35, 10, v34
	v_cmp_gt_i32_e64 s[44:45], s85, v35
	v_or_b32_e32 v35, 42, v34
	v_cmp_gt_i32_e64 s[12:13], s85, v35
	v_or_b32_e32 v35, 11, v34
	v_cmp_gt_i32_e64 s[46:47], s85, v35
	v_or_b32_e32 v35, 43, v34
	v_cmp_gt_i32_e64 s[14:15], s85, v35
	v_or_b32_e32 v35, 16, v34
	v_cmp_gt_i32_e64 s[48:49], s85, v35
	v_or_b32_e32 v35, 48, v34
	v_cmp_gt_i32_e64 s[16:17], s85, v35
	v_or_b32_e32 v35, 17, v34
	v_cmp_gt_i32_e64 s[50:51], s85, v35
	v_or_b32_e32 v35, 49, v34
	v_cmp_gt_i32_e64 s[18:19], s85, v35
	v_or_b32_e32 v35, 18, v34
	v_cmp_gt_i32_e64 s[52:53], s85, v35
	v_or_b32_e32 v35, 50, v34
	v_cmp_gt_i32_e64 s[20:21], s85, v35
	v_or_b32_e32 v35, 19, v34
	v_cmp_gt_i32_e64 s[54:55], s85, v35
	v_or_b32_e32 v35, 51, v34
	v_cmp_gt_i32_e64 s[22:23], s85, v35
	v_or_b32_e32 v35, 24, v34
	v_cmp_gt_i32_e64 s[56:57], s85, v35
	v_or_b32_e32 v35, 56, v34
	v_cmp_gt_i32_e64 s[24:25], s85, v35
	v_or_b32_e32 v35, 25, v34
	v_cmp_gt_i32_e64 s[58:59], s85, v35
	v_or_b32_e32 v35, 57, v34
	v_cmp_gt_i32_e64 s[28:29], s85, v35
	v_or_b32_e32 v35, 26, v34
	v_cmp_gt_i32_e64 s[60:61], s85, v35
	v_or_b32_e32 v35, 58, v34
	v_cmp_gt_i32_e64 s[34:35], s85, v35
	v_or_b32_e32 v35, 27, v34
	v_cmp_gt_i32_e64 s[62:63], s85, v35
	s_or_b64 s[60:61], s[62:63], s[60:61]
	s_or_b64 s[58:59], s[60:61], s[58:59]
	s_or_b64 s[56:57], s[58:59], s[56:57]
	s_or_b64 s[54:55], s[56:57], s[54:55]
	s_or_b64 s[52:53], s[54:55], s[52:53]
	s_or_b64 s[50:51], s[52:53], s[50:51]
	s_or_b64 s[48:49], s[50:51], s[48:49]
	s_or_b64 s[46:47], s[48:49], s[46:47]
	s_or_b64 s[44:45], s[46:47], s[44:45]
	s_or_b64 s[42:43], s[44:45], s[42:43]
	s_or_b64 s[40:41], s[42:43], s[40:41]
	s_or_b64 s[38:39], s[40:41], s[38:39]
	s_or_b64 s[36:37], s[38:39], s[36:37]
	v_cmp_gt_i32_e64 s[26:27], s85, v34
	s_or_b64 s[30:31], s[36:37], s[30:31]
	v_mov_b32_e32 v36, 0xff800000
	s_or_b64 s[26:27], s[30:31], s[26:27]
	v_or_b32_e32 v34, 59, v34
	v_cndmask_b32_e64 v18, v36, v18, s[26:27]
	v_cmp_gt_i32_e64 s[26:27], s85, v34
	v_cndmask_b32_e64 v33, v36, v33, s[62:63]
	v_cndmask_b32_e64 v32, v36, v32, s[60:61]
	v_cndmask_b32_e64 v17, v36, v17, s[26:27]
	s_or_b64 s[26:27], s[26:27], s[34:35]
	v_cndmask_b32_e64 v16, v36, v16, s[26:27]
	s_or_b64 s[26:27], s[26:27], s[28:29]
	s_or_b64 s[24:25], s[26:27], s[24:25]
	s_or_b64 s[22:23], s[24:25], s[22:23]
	s_or_b64 s[20:21], s[22:23], s[20:21]
	s_or_b64 s[18:19], s[20:21], s[18:19]
	s_or_b64 s[16:17], s[18:19], s[16:17]
	s_or_b64 s[14:15], s[16:17], s[14:15]
	s_or_b64 s[12:13], s[14:15], s[12:13]
	s_or_b64 s[10:11], s[12:13], s[10:11]
	s_or_b64 s[8:9], s[10:11], s[8:9]
	s_or_b64 s[6:7], s[8:9], s[6:7]
	s_or_b64 s[4:5], s[6:7], s[4:5]
	s_or_b64 s[2:3], s[4:5], s[2:3]
	s_or_b64 vcc, s[2:3], vcc
	v_cndmask_b32_e64 v31, v36, v31, s[58:59]
	v_cndmask_b32_e64 v30, v36, v30, s[56:57]
	v_cndmask_b32_e64 v29, v36, v29, s[54:55]
	v_cndmask_b32_e64 v28, v36, v28, s[52:53]
	v_cndmask_b32_e64 v27, v36, v27, s[50:51]
	v_cndmask_b32_e64 v26, v36, v26, s[48:49]
	v_cndmask_b32_e64 v25, v36, v25, s[46:47]
	v_cndmask_b32_e64 v24, v36, v24, s[44:45]
	v_cndmask_b32_e64 v23, v36, v23, s[42:43]
	v_cndmask_b32_e64 v22, v36, v22, s[40:41]
	v_cndmask_b32_e64 v21, v36, v21, s[38:39]
	v_cndmask_b32_e64 v20, v36, v20, s[36:37]
	v_cndmask_b32_e64 v19, v36, v19, s[30:31]
	v_cndmask_b32_e64 v15, v36, v15, s[26:27]
	v_cndmask_b32_e64 v14, v36, v14, s[24:25]
	v_cndmask_b32_e64 v13, v36, v13, s[22:23]
	v_cndmask_b32_e64 v12, v36, v12, s[20:21]
	v_cndmask_b32_e64 v11, v36, v11, s[18:19]
	v_cndmask_b32_e64 v10, v36, v10, s[16:17]
	v_cndmask_b32_e64 v9, v36, v9, s[14:15]
	v_cndmask_b32_e64 v8, v36, v8, s[12:13]
	v_cndmask_b32_e64 v7, v36, v7, s[10:11]
	v_cndmask_b32_e64 v6, v36, v6, s[8:9]
	v_cndmask_b32_e64 v5, v36, v5, s[6:7]
	v_cndmask_b32_e64 v4, v36, v4, s[4:5]
	v_cndmask_b32_e64 v3, v36, v3, s[2:3]
	v_cndmask_b32_e32 v2, v36, v2, vcc
